# FFN-in sixth round computed by workgroup pairs with split-K (half the k-steps each), accumulator halves swapped through d_ws with sc1 stores/loads, PP tail one unit per workgroup
# baseline (speedup 1.0000x reference)
_Z8mega_fwd4Args:
	s_mov_b32 s7, 0
	v_writelane_b32 v255, s7, 62
	v_readfirstlane_b32 s7, v0
	s_bfe_u32 s7, s7, 0x10008
	v_writelane_b32 v255, s7, 63
	s_load_dword s3, s[0:1], 0xc0
	s_add_u32 s4, s0, 0xc0
	v_writelane_b32 v254, s0, 0
	s_addc_u32 s5, s1, 0
	s_nop 0
	v_writelane_b32 v254, s1, 1
	v_writelane_b32 v254, s4, 2
	s_waitcnt lgkmcnt(0)
	s_and_b32 s0, s3, 7
	s_cmp_lg_u32 s0, 0
	v_writelane_b32 v254, s5, 3
	v_writelane_b32 v254, s3, 4
	v_writelane_b32 v254, s2, 5
	v_writelane_b32 v254, s2, 6
	s_cbranch_scc1 .LBB0_2
	v_readlane_b32 s3, v254, 5
	s_ashr_i32 s1, s3, 31
	s_lshr_b32 s1, s1, 29
	s_add_i32 s1, s3, s1
	v_readlane_b32 s0, v254, 4
	s_ashr_i32 s2, s1, 3
	s_and_b32 s1, s1, -8
	s_ashr_i32 s0, s0, 3
	s_sub_i32 s1, s3, s1
	s_mul_i32 s0, s0, s1
	s_add_i32 s0, s0, s2
	v_writelane_b32 v254, s0, 6

.LBB0_222:
	v_readlane_b32 s6, v254, 37
	s_add_i32 s83, s83, 1
	v_readlane_b32 s7, v254, 38
	s_mul_i32 s6, s83, s6
	v_readlane_b32 s7, v254, 31
	s_add_i32 s6, s6, s7
	v_readlane_b32 s98, v254, 37
	s_cmp_eq_u32 s98, 0x100
	s_cselect_b32 s98, 1, 0
	s_lshr_b32 s99, s7, 7
	s_add_i32 s99, s99, 1
	s_cmp_eq_u32 s83, 6
	s_cselect_b32 s32, s99, 0
	s_mul_i32 s32, s32, s98
	s_cmp_eq_u32 s83, 5
	s_cselect_b32 s99, 0x80, 0
	s_mul_i32 s99, s99, s98
	s_and_b32 s98, s6, s99
	s_andn2_b32 s6, s6, s99
	s_lshl_b32 s99, s98, 3
	s_cmpk_lt_u32 s6, 0x580
	s_cselect_b64 s[38:39], -1, 0
	s_cmpk_gt_u32 s6, 0x57f
	s_cbranch_scc1 .LBB0_224
	s_and_b32 s7, s6, 7
	s_lshr_b32 s14, s6, 3
	s_mulk_i32 s7, 0xb0
	s_add_i32 s7, s7, s14
	s_mul_hi_u32 s14, s7, 0xba2e8c
	s_mul_i32 s15, s14, 0xfffffea0
	s_add_i32 s15, s15, s7
	s_lshl_b32 s7, s14, 3
	s_bfe_u32 s6, s6, 0x30003
	s_or_b32 s85, s7, s6
	s_lshr_b32 s22, s15, 3
.LBB0_224:
	ds_read_b128 v[2:5], v169
	ds_read_b128 v[6:9], v169 offset:1024
	ds_read_b128 v[10:13], v169 offset:2048
	ds_read_b128 v[14:17], v169 offset:3072
	ds_read_b128 v[18:21], v170
	ds_read_b128 v[22:25], v170 offset:1024
	ds_read_b128 v[26:29], v170 offset:2048
	ds_read_b128 v[30:33], v170 offset:3072
	s_lshl_b32 s43, s85, 19
	s_lshl_b32 s52, s22, 19
	s_add_i32 s43, s43, s99
	s_add_i32 s52, s52, s99
	s_or_b32 s15, s29, 0x80
	s_or_b32 s62, s28, 0x100
	s_and_b64 s[6:7], s[38:39], exec
	s_cselect_b32 vcc_lo, s43, s29
	s_or_b32 s14, s29, 0x100
	s_and_b64 s[6:7], s[38:39], exec
	s_cselect_b32 vcc_hi, s52, s28
	s_mov_b32 m0, s79
	ds_read_b128 v[34:37], v171
	ds_read_b128 v[38:41], v171 offset:1024
	ds_read_b128 v[42:45], v171 offset:2048
	ds_read_b128 v[46:49], v171 offset:3072
	ds_read_b128 v[50:53], v171 offset:4096
	ds_read_b128 v[54:57], v171 offset:5120
	ds_read_b128 v[58:61], v171 offset:6144
	ds_read_b128 v[62:65], v171 offset:7168
	buffer_load_dwordx4 v163, s[64:67], s15 offen lds
	s_mov_b32 m0, s81
	s_or_b32 s6, s29, 0x40080
	buffer_load_dwordx4 v165, s[64:67], s15 offen lds
	s_mov_b32 m0, s80
	s_nop 0
	buffer_load_dwordx4 v163, s[64:67], s6 offen lds
	s_mov_b32 m0, s82
	s_nop 0
	buffer_load_dwordx4 v165, s[64:67], s6 offen lds
	s_waitcnt vmcnt(8)
	s_waitcnt lgkmcnt(0)
	s_barrier
	s_setprio 1
	s_waitcnt lgkmcnt(6)
	v_mfma_scale_f32_16x16x128_f8f6f4 v[150:153], v[2:9], v[34:41], 0, v234, v234 op_sel_hi:[0,0,0]
	v_mfma_scale_f32_16x16x128_f8f6f4 v[146:149], v[10:17], v[34:41], 0, v234, v234 op_sel_hi:[0,0,0]
	s_waitcnt vmcnt(17) lgkmcnt(4)
	v_mfma_scale_f32_16x16x128_f8f6f4 v[134:137], v[2:9], v[42:49], 0, v234, v234 op_sel_hi:[0,0,0]
	v_mfma_scale_f32_16x16x128_f8f6f4 v[130:133], v[10:17], v[42:49], 0, v234, v234 op_sel_hi:[0,0,0]
	s_waitcnt lgkmcnt(2)
	v_mfma_scale_f32_16x16x128_f8f6f4 v[118:121], v[2:9], v[50:57], 0, v234, v234 op_sel_hi:[0,0,0]
	v_mfma_scale_f32_16x16x128_f8f6f4 v[114:117], v[10:17], v[50:57], 0, v234, v234 op_sel_hi:[0,0,0]
	s_waitcnt lgkmcnt(0)
	v_mfma_scale_f32_16x16x128_f8f6f4 v[98:101], v[2:9], v[58:65], 0, v234, v234 op_sel_hi:[0,0,0]
	v_mfma_scale_f32_16x16x128_f8f6f4 v[90:93], v[10:17], v[58:65], 0, v234, v234 op_sel_hi:[0,0,0]
	v_mfma_scale_f32_16x16x128_f8f6f4 v[158:161], v[18:25], v[34:41], 0, v234, v234 op_sel_hi:[0,0,0]
	v_mfma_scale_f32_16x16x128_f8f6f4 v[154:157], v[26:33], v[34:41], 0, v234, v234 op_sel_hi:[0,0,0]
	v_mfma_scale_f32_16x16x128_f8f6f4 v[142:145], v[18:25], v[42:49], 0, v234, v234 op_sel_hi:[0,0,0]
	s_waitcnt vmcnt(16)
	v_mfma_scale_f32_16x16x128_f8f6f4 v[138:141], v[26:33], v[42:49], 0, v234, v234 op_sel_hi:[0,0,0]
	v_mfma_scale_f32_16x16x128_f8f6f4 v[126:129], v[18:25], v[50:57], 0, v234, v234 op_sel_hi:[0,0,0]
	v_mfma_scale_f32_16x16x128_f8f6f4 v[122:125], v[26:33], v[50:57], 0, v234, v234 op_sel_hi:[0,0,0]
	v_mfma_scale_f32_16x16x128_f8f6f4 v[110:113], v[18:25], v[58:65], 0, v234, v234 op_sel_hi:[0,0,0]
	v_mfma_scale_f32_16x16x128_f8f6f4 v[106:109], v[26:33], v[58:65], 0, v234, v234 op_sel_hi:[0,0,0]
	s_setprio 0
	s_barrier
	s_mov_b32 m0, s9
	s_mov_b32 s6, s66
	s_mov_b32 s7, s67
	ds_read_b128 v[74:77], v171 offset:16384
	ds_read_b128 v[78:81], v171 offset:17408
	ds_read_b128 v[174:177], v171 offset:18432
	ds_read_b128 v[178:181], v171 offset:19456
	ds_read_b128 v[182:185], v171 offset:20480
	ds_read_b128 v[186:189], v171 offset:21504
	ds_read_b128 v[190:193], v171 offset:22528
	ds_read_b128 v[194:197], v171 offset:23552
	buffer_load_dwordx4 v164, s[4:7], s62 offen lds
	s_mov_b32 m0, s10
	s_or_b32 s15, s28, 0x40100
	buffer_load_dwordx4 v166, s[4:7], s62 offen lds
	s_mov_b32 m0, s11
	s_nop 0
	buffer_load_dwordx4 v164, s[4:7], s15 offen lds
	s_mov_b32 m0, s12
	s_nop 0
	buffer_load_dwordx4 v166, s[4:7], s15 offen lds
	s_waitcnt vmcnt(6)
	s_waitcnt lgkmcnt(0)
	s_barrier
	s_setprio 1
	s_waitcnt lgkmcnt(6)
	v_mfma_scale_f32_16x16x128_f8f6f4 v[86:89], v[2:9], v[74:81], 0, v234, v234 op_sel_hi:[0,0,0]
	v_mfma_scale_f32_16x16x128_f8f6f4 v[82:85], v[10:17], v[74:81], 0, v234, v234 op_sel_hi:[0,0,0]
	s_waitcnt lgkmcnt(4)
	v_mfma_scale_f32_16x16x128_f8f6f4 v[70:73], v[2:9], v[174:181], 0, v234, v234 op_sel_hi:[0,0,0]
	v_mfma_scale_f32_16x16x128_f8f6f4 v[66:69], v[10:17], v[174:181], 0, v234, v234 op_sel_hi:[0,0,0]
	s_waitcnt lgkmcnt(2)
	v_mfma_scale_f32_16x16x128_f8f6f4 v[58:61], v[2:9], v[182:189], 0, v234, v234 op_sel_hi:[0,0,0]
	v_mfma_scale_f32_16x16x128_f8f6f4 v[50:53], v[10:17], v[182:189], 0, v234, v234 op_sel_hi:[0,0,0]
	s_waitcnt lgkmcnt(0)
	v_mfma_scale_f32_16x16x128_f8f6f4 v[42:45], v[2:9], v[190:197], 0, v234, v234 op_sel_hi:[0,0,0]
	v_mfma_scale_f32_16x16x128_f8f6f4 v[34:37], v[10:17], v[190:197], 0, v234, v234 op_sel_hi:[0,0,0]
	v_mfma_scale_f32_16x16x128_f8f6f4 v[102:105], v[18:25], v[74:81], 0, v234, v234 op_sel_hi:[0,0,0]
	v_mfma_scale_f32_16x16x128_f8f6f4 v[94:97], v[26:33], v[74:81], 0, v234, v234 op_sel_hi:[0,0,0]
	v_mfma_scale_f32_16x16x128_f8f6f4 v[78:81], v[18:25], v[174:181], 0, v234, v234 op_sel_hi:[0,0,0]
	v_mfma_scale_f32_16x16x128_f8f6f4 v[74:77], v[26:33], v[174:181], 0, v234, v234 op_sel_hi:[0,0,0]
	v_mfma_scale_f32_16x16x128_f8f6f4 v[62:65], v[18:25], v[182:189], 0, v234, v234 op_sel_hi:[0,0,0]
	v_mfma_scale_f32_16x16x128_f8f6f4 v[54:57], v[26:33], v[182:189], 0, v234, v234 op_sel_hi:[0,0,0]
	v_mfma_scale_f32_16x16x128_f8f6f4 v[46:49], v[18:25], v[190:197], 0, v234, v234 op_sel_hi:[0,0,0]
	v_mfma_scale_f32_16x16x128_f8f6f4 v[38:41], v[26:33], v[190:197], 0, v234, v234 op_sel_hi:[0,0,0]
	s_setprio 0
	s_barrier
	ds_read_b128 v[26:29], v172
	ds_read_b128 v[30:33], v172 offset:1024
	ds_read_b128 v[18:21], v172 offset:2048
	ds_read_b128 v[22:25], v172 offset:3072
	ds_read_b128 v[10:13], v173
	ds_read_b128 v[14:17], v173 offset:1024
	ds_read_b128 v[2:5], v173 offset:2048
	ds_read_b128 v[6:9], v173 offset:3072
	s_mov_b32 m0, s8
	ds_read_b128 v[174:177], v171 offset:32768
	ds_read_b128 v[178:181], v171 offset:33792
	ds_read_b128 v[182:185], v171 offset:34816
	ds_read_b128 v[186:189], v171 offset:35840
	ds_read_b128 v[190:193], v171 offset:36864
	ds_read_b128 v[194:197], v171 offset:37888
	ds_read_b128 v[204:207], v171 offset:38912
	ds_read_b128 v[208:211], v171 offset:39936
	buffer_load_dwordx4 v163, s[64:67], s14 offen lds
	s_mov_b32 m0, s13
	s_nop 0
	buffer_load_dwordx4 v165, s[64:67], s14 offen lds
	s_or_b32 s14, s29, 0x40100
	s_mov_b32 m0, s20
	s_nop 0
	buffer_load_dwordx4 v163, s[64:67], s14 offen lds
	s_mov_b32 m0, s21
	s_nop 0
	buffer_load_dwordx4 v165, s[64:67], s14 offen lds
	s_waitcnt vmcnt(8)
	s_waitcnt lgkmcnt(0)
	s_barrier
	s_setprio 1
	s_waitcnt lgkmcnt(6)
	v_mfma_scale_f32_16x16x128_f8f6f4 v[150:153], v[26:33], v[174:181], v[150:153], v234, v234 op_sel_hi:[0,0,0]
	v_mfma_scale_f32_16x16x128_f8f6f4 v[146:149], v[18:25], v[174:181], v[146:149], v234, v234 op_sel_hi:[0,0,0]
	s_waitcnt lgkmcnt(4)
	v_mfma_scale_f32_16x16x128_f8f6f4 v[134:137], v[26:33], v[182:189], v[134:137], v234, v234 op_sel_hi:[0,0,0]
	v_mfma_scale_f32_16x16x128_f8f6f4 v[130:133], v[18:25], v[182:189], v[130:133], v234, v234 op_sel_hi:[0,0,0]
	s_waitcnt lgkmcnt(2)
	v_mfma_scale_f32_16x16x128_f8f6f4 v[118:121], v[26:33], v[190:197], v[118:121], v234, v234 op_sel_hi:[0,0,0]
	v_mfma_scale_f32_16x16x128_f8f6f4 v[114:117], v[18:25], v[190:197], v[114:117], v234, v234 op_sel_hi:[0,0,0]
	s_waitcnt lgkmcnt(0)
	v_mfma_scale_f32_16x16x128_f8f6f4 v[98:101], v[26:33], v[204:211], v[98:101], v234, v234 op_sel_hi:[0,0,0]
	v_mfma_scale_f32_16x16x128_f8f6f4 v[90:93], v[18:25], v[204:211], v[90:93], v234, v234 op_sel_hi:[0,0,0]
	v_mfma_scale_f32_16x16x128_f8f6f4 v[158:161], v[10:17], v[174:181], v[158:161], v234, v234 op_sel_hi:[0,0,0]
	v_mfma_scale_f32_16x16x128_f8f6f4 v[154:157], v[2:9], v[174:181], v[154:157], v234, v234 op_sel_hi:[0,0,0]
	v_mfma_scale_f32_16x16x128_f8f6f4 v[142:145], v[10:17], v[182:189], v[142:145], v234, v234 op_sel_hi:[0,0,0]
	v_mfma_scale_f32_16x16x128_f8f6f4 v[138:141], v[2:9], v[182:189], v[138:141], v234, v234 op_sel_hi:[0,0,0]
	v_mfma_scale_f32_16x16x128_f8f6f4 v[126:129], v[10:17], v[190:197], v[126:129], v234, v234 op_sel_hi:[0,0,0]
	v_mfma_scale_f32_16x16x128_f8f6f4 v[122:125], v[2:9], v[190:197], v[122:125], v234, v234 op_sel_hi:[0,0,0]
	v_mfma_scale_f32_16x16x128_f8f6f4 v[110:113], v[10:17], v[204:211], v[110:113], v234, v234 op_sel_hi:[0,0,0]
	v_mfma_scale_f32_16x16x128_f8f6f4 v[106:109], v[2:9], v[204:211], v[106:109], v234, v234 op_sel_hi:[0,0,0]
	s_setprio 0
	s_barrier
	s_mov_b32 m0, s26
	s_or_b32 s14, s28, 0x180
	ds_read_b128 v[174:177], v171 offset:49152
	ds_read_b128 v[178:181], v171 offset:50176
	ds_read_b128 v[182:185], v171 offset:51200
	ds_read_b128 v[186:189], v171 offset:52224
	ds_read_b128 v[190:193], v171 offset:53248
	ds_read_b128 v[194:197], v171 offset:54272
	ds_read_b128 v[204:207], v171 offset:55296
	ds_read_b128 v[208:211], v171 offset:56320
	buffer_load_dwordx4 v164, s[4:7], s14 offen lds
	s_mov_b32 m0, s27
	s_nop 0
	buffer_load_dwordx4 v166, s[4:7], s14 offen lds
	s_or_b32 s14, s28, 0x40180
	s_mov_b32 m0, s40
	s_nop 0
	buffer_load_dwordx4 v164, s[4:7], s14 offen lds
	s_mov_b32 m0, s76
	s_nop 0
	buffer_load_dwordx4 v166, s[4:7], s14 offen lds
	s_waitcnt vmcnt(6)
	s_waitcnt lgkmcnt(0)
	s_barrier
	s_setprio 1
	s_waitcnt lgkmcnt(6)
	v_mfma_scale_f32_16x16x128_f8f6f4 v[86:89], v[26:33], v[174:181], v[86:89], v234, v234 op_sel_hi:[0,0,0]
	v_mfma_scale_f32_16x16x128_f8f6f4 v[82:85], v[18:25], v[174:181], v[82:85], v234, v234 op_sel_hi:[0,0,0]
	s_waitcnt lgkmcnt(4)
	v_mfma_scale_f32_16x16x128_f8f6f4 v[70:73], v[26:33], v[182:189], v[70:73], v234, v234 op_sel_hi:[0,0,0]
	v_mfma_scale_f32_16x16x128_f8f6f4 v[66:69], v[18:25], v[182:189], v[66:69], v234, v234 op_sel_hi:[0,0,0]
	s_waitcnt lgkmcnt(2)
	v_mfma_scale_f32_16x16x128_f8f6f4 v[58:61], v[26:33], v[190:197], v[58:61], v234, v234 op_sel_hi:[0,0,0]
	v_mfma_scale_f32_16x16x128_f8f6f4 v[50:53], v[18:25], v[190:197], v[50:53], v234, v234 op_sel_hi:[0,0,0]
	s_waitcnt lgkmcnt(0)
	v_mfma_scale_f32_16x16x128_f8f6f4 v[42:45], v[26:33], v[204:211], v[42:45], v234, v234 op_sel_hi:[0,0,0]
	v_mfma_scale_f32_16x16x128_f8f6f4 v[34:37], v[18:25], v[204:211], v[34:37], v234, v234 op_sel_hi:[0,0,0]
	v_mfma_scale_f32_16x16x128_f8f6f4 v[102:105], v[10:17], v[174:181], v[102:105], v234, v234 op_sel_hi:[0,0,0]
	v_mfma_scale_f32_16x16x128_f8f6f4 v[94:97], v[2:9], v[174:181], v[94:97], v234, v234 op_sel_hi:[0,0,0]
	v_mfma_scale_f32_16x16x128_f8f6f4 v[78:81], v[10:17], v[182:189], v[78:81], v234, v234 op_sel_hi:[0,0,0]
	v_mfma_scale_f32_16x16x128_f8f6f4 v[74:77], v[2:9], v[182:189], v[74:77], v234, v234 op_sel_hi:[0,0,0]
	v_mfma_scale_f32_16x16x128_f8f6f4 v[62:65], v[10:17], v[190:197], v[62:65], v234, v234 op_sel_hi:[0,0,0]
	v_mfma_scale_f32_16x16x128_f8f6f4 v[54:57], v[2:9], v[190:197], v[54:57], v234, v234 op_sel_hi:[0,0,0]
	v_mfma_scale_f32_16x16x128_f8f6f4 v[46:49], v[10:17], v[204:211], v[46:49], v234, v234 op_sel_hi:[0,0,0]
	v_mfma_scale_f32_16x16x128_f8f6f4 v[38:41], v[2:9], v[204:211], v[38:41], v234, v234 op_sel_hi:[0,0,0]
	s_setprio 0
	s_barrier
	s_addk_i32 s28, 0x200
	s_add_i32 s29, s29, 0x40180
	s_cmp_lg_u32 s32, 0
	s_cselect_b32 s62, 8, 0

.LBB0_228:
	s_cmp_eq_u32 s32, 0
	s_cbranch_scc1 .Lxk_done
	s_getreg_b32 s98, hwreg(HW_REG_HW_ID, 0, 6)
	s_and_b32 s98, s98, 63
	s_lshl_b32 s98, s98, 2
	s_or_b32 s98, s98, 0x20400
	v_mov_b32_e32 v2, s98
	ds_read_b32 v2, v2
	v_mbcnt_lo_u32_b32 v3, -1, 0
	v_mbcnt_hi_u32_b32 v3, -1, v3
	s_waitcnt lgkmcnt(0)
	v_readfirstlane_b32 s98, v2
	s_nop 3
	v_lshl_or_b32 v3, s98, 6, v3
	v_lshlrev_b32_e32 v3, 4, v3
	v_readlane_b32 s14, v254, 31
	s_and_b32 s14, s14, 0x7f
	s_lshl_b32 s15, s14, 18
	s_add_u32 s6, s34, 0x5800000
	s_addc_u32 s7, s35, 0
	s_add_u32 s6, s6, s15
	s_addc_u32 s7, s7, 0
	v_readlane_b32 s99, v255, 62
	s_add_i32 s99, s99, 1
	s_nop 0
	v_writelane_b32 v255, s99, 62
	s_cmp_eq_u32 s32, 2
	s_cbranch_scc1 .Lxk_s2
	s_add_u32 s6, s6, 0x20000
	s_addc_u32 s7, s7, 0
	global_store_dwordx4 v3, v[34:37], s[6:7] sc1
	s_add_u32 s6, s6, 0x2000
	s_addc_u32 s7, s7, 0
	global_store_dwordx4 v3, v[38:41], s[6:7] sc1
	s_add_u32 s6, s6, 0x2000
	s_addc_u32 s7, s7, 0
	global_store_dwordx4 v3, v[42:45], s[6:7] sc1
	s_add_u32 s6, s6, 0x2000
	s_addc_u32 s7, s7, 0
	global_store_dwordx4 v3, v[46:49], s[6:7] sc1
	s_add_u32 s6, s6, 0x2000
	s_addc_u32 s7, s7, 0
	global_store_dwordx4 v3, v[50:53], s[6:7] sc1
	s_add_u32 s6, s6, 0x2000
	s_addc_u32 s7, s7, 0
	global_store_dwordx4 v3, v[54:57], s[6:7] sc1
	s_add_u32 s6, s6, 0x2000
	s_addc_u32 s7, s7, 0
	global_store_dwordx4 v3, v[58:61], s[6:7] sc1
	s_add_u32 s6, s6, 0x2000
	s_addc_u32 s7, s7, 0
	global_store_dwordx4 v3, v[62:65], s[6:7] sc1
	s_add_u32 s6, s6, 0x2000
	s_addc_u32 s7, s7, 0
	global_store_dwordx4 v3, v[66:69], s[6:7] sc1
	s_add_u32 s6, s6, 0x2000
	s_addc_u32 s7, s7, 0
	global_store_dwordx4 v3, v[70:73], s[6:7] sc1
	s_add_u32 s6, s6, 0x2000
	s_addc_u32 s7, s7, 0
	global_store_dwordx4 v3, v[74:77], s[6:7] sc1
	s_add_u32 s6, s6, 0x2000
	s_addc_u32 s7, s7, 0
	global_store_dwordx4 v3, v[78:81], s[6:7] sc1
	s_add_u32 s6, s6, 0x2000
	s_addc_u32 s7, s7, 0
	global_store_dwordx4 v3, v[82:85], s[6:7] sc1
	s_add_u32 s6, s6, 0x2000
	s_addc_u32 s7, s7, 0
	global_store_dwordx4 v3, v[86:89], s[6:7] sc1
	s_add_u32 s6, s6, 0x2000
	s_addc_u32 s7, s7, 0
	global_store_dwordx4 v3, v[94:97], s[6:7] sc1
	s_add_u32 s6, s6, 0x2000
	s_addc_u32 s7, s7, 0
	global_store_dwordx4 v3, v[102:105], s[6:7] sc1
	s_add_u32 s6, s6, 0x2000
	s_addc_u32 s7, s7, 0
	s_sub_u32 s6, s6, 0x40000
	s_subb_u32 s7, s7, 0
	s_branch .Lxk_sync
.Lxk_s2:
	global_store_dwordx4 v3, v[90:93], s[6:7] sc1
	s_add_u32 s6, s6, 0x2000
	s_addc_u32 s7, s7, 0
	global_store_dwordx4 v3, v[98:101], s[6:7] sc1
	s_add_u32 s6, s6, 0x2000
	s_addc_u32 s7, s7, 0
	global_store_dwordx4 v3, v[106:109], s[6:7] sc1
	s_add_u32 s6, s6, 0x2000
	s_addc_u32 s7, s7, 0
	global_store_dwordx4 v3, v[110:113], s[6:7] sc1
	s_add_u32 s6, s6, 0x2000
	s_addc_u32 s7, s7, 0
	global_store_dwordx4 v3, v[114:117], s[6:7] sc1
	s_add_u32 s6, s6, 0x2000
	s_addc_u32 s7, s7, 0
	global_store_dwordx4 v3, v[118:121], s[6:7] sc1
	s_add_u32 s6, s6, 0x2000
	s_addc_u32 s7, s7, 0
	global_store_dwordx4 v3, v[122:125], s[6:7] sc1
	s_add_u32 s6, s6, 0x2000
	s_addc_u32 s7, s7, 0
	global_store_dwordx4 v3, v[126:129], s[6:7] sc1
	s_add_u32 s6, s6, 0x2000
	s_addc_u32 s7, s7, 0
	global_store_dwordx4 v3, v[130:133], s[6:7] sc1
	s_add_u32 s6, s6, 0x2000
	s_addc_u32 s7, s7, 0
	global_store_dwordx4 v3, v[134:137], s[6:7] sc1
	s_add_u32 s6, s6, 0x2000
	s_addc_u32 s7, s7, 0
	global_store_dwordx4 v3, v[138:141], s[6:7] sc1
	s_add_u32 s6, s6, 0x2000
	s_addc_u32 s7, s7, 0
	global_store_dwordx4 v3, v[142:145], s[6:7] sc1
	s_add_u32 s6, s6, 0x2000
	s_addc_u32 s7, s7, 0
	global_store_dwordx4 v3, v[146:149], s[6:7] sc1
	s_add_u32 s6, s6, 0x2000
	s_addc_u32 s7, s7, 0
	global_store_dwordx4 v3, v[150:153], s[6:7] sc1
	s_add_u32 s6, s6, 0x2000
	s_addc_u32 s7, s7, 0
	global_store_dwordx4 v3, v[154:157], s[6:7] sc1
	s_add_u32 s6, s6, 0x2000
	s_addc_u32 s7, s7, 0
	global_store_dwordx4 v3, v[158:161], s[6:7] sc1
	s_add_u32 s6, s6, 0x2000
	s_addc_u32 s7, s7, 0
	s_sub_u32 s6, s6, 0x20000
	s_subb_u32 s7, s7, 0
.Lxk_sync:
	s_waitcnt vmcnt(0)
	s_barrier
	s_cmp_lg_u32 s98, 0
	s_cbranch_scc1 .Lxk_wait
	s_mov_b64 vcc, exec
	s_mov_b64 exec, 1
	s_sub_u32 s62, s34, 0x34e00000
	s_subb_u32 s63, s35, 0
	s_lshl_b32 s15, s14, 6
	s_add_u32 s62, s62, s15
	s_addc_u32 s63, s63, 0
	s_add_u32 s62, s62, 0x10000
	s_addc_u32 s63, s63, 0
	s_sub_i32 s15, s32, 1
	s_lshl_b32 s15, s15, 5
	v_mov_b32_e32 v4, s15
	s_sub_i32 s15, 2, s32
	s_lshl_b32 s15, s15, 5
	v_mov_b32_e32 v6, s15
	v_mov_b32_e32 v5, 1
	global_atomic_add v4, v5, s[62:63]
	s_mov_b32 s15, 0
.Lxk_spin:
	global_load_dword v7, v6, s[62:63] sc1
	s_waitcnt vmcnt(0)
	v_readfirstlane_b32 s14, v7
	s_cmp_ge_u32 s14, s99
	s_cbranch_scc1 .Lxk_got
	s_sleep 1
	s_add_i32 s15, s15, 1
	s_cmp_lt_u32 s15, 0x4000
	s_cbranch_scc1 .Lxk_spin
.Lxk_got:
	s_mov_b64 exec, vcc
.Lxk_wait:
	s_barrier
	s_cmp_eq_u32 s32, 2
	s_cbranch_scc1 .Lxk_l2
	global_load_dwordx4 v[34:37], v3, s[6:7] sc1
	s_add_u32 s6, s6, 0x2000
	s_addc_u32 s7, s7, 0
	global_load_dwordx4 v[38:41], v3, s[6:7] sc1
	s_add_u32 s6, s6, 0x2000
	s_addc_u32 s7, s7, 0
	global_load_dwordx4 v[42:45], v3, s[6:7] sc1
	s_add_u32 s6, s6, 0x2000
	s_addc_u32 s7, s7, 0
	global_load_dwordx4 v[46:49], v3, s[6:7] sc1
	s_add_u32 s6, s6, 0x2000
	s_addc_u32 s7, s7, 0
	global_load_dwordx4 v[50:53], v3, s[6:7] sc1
	s_add_u32 s6, s6, 0x2000
	s_addc_u32 s7, s7, 0
	global_load_dwordx4 v[54:57], v3, s[6:7] sc1
	s_add_u32 s6, s6, 0x2000
	s_addc_u32 s7, s7, 0
	global_load_dwordx4 v[58:61], v3, s[6:7] sc1
	s_add_u32 s6, s6, 0x2000
	s_addc_u32 s7, s7, 0
	global_load_dwordx4 v[62:65], v3, s[6:7] sc1
	s_add_u32 s6, s6, 0x2000
	s_addc_u32 s7, s7, 0
	global_load_dwordx4 v[66:69], v3, s[6:7] sc1
	s_add_u32 s6, s6, 0x2000
	s_addc_u32 s7, s7, 0
	global_load_dwordx4 v[70:73], v3, s[6:7] sc1
	s_add_u32 s6, s6, 0x2000
	s_addc_u32 s7, s7, 0
	global_load_dwordx4 v[74:77], v3, s[6:7] sc1
	s_add_u32 s6, s6, 0x2000
	s_addc_u32 s7, s7, 0
	global_load_dwordx4 v[78:81], v3, s[6:7] sc1
	s_add_u32 s6, s6, 0x2000
	s_addc_u32 s7, s7, 0
	global_load_dwordx4 v[82:85], v3, s[6:7] sc1
	s_add_u32 s6, s6, 0x2000
	s_addc_u32 s7, s7, 0
	global_load_dwordx4 v[86:89], v3, s[6:7] sc1
	s_add_u32 s6, s6, 0x2000
	s_addc_u32 s7, s7, 0
	global_load_dwordx4 v[94:97], v3, s[6:7] sc1
	s_add_u32 s6, s6, 0x2000
	s_addc_u32 s7, s7, 0
	global_load_dwordx4 v[102:105], v3, s[6:7] sc1
	s_add_u32 s6, s6, 0x2000
	s_addc_u32 s7, s7, 0
	s_waitcnt vmcnt(0)
	v_pk_add_f32 v[90:91], v[90:91], v[34:35]
	v_pk_add_f32 v[92:93], v[92:93], v[36:37]
	v_pk_add_f32 v[98:99], v[98:99], v[38:39]
	v_pk_add_f32 v[100:101], v[100:101], v[40:41]
	v_pk_add_f32 v[106:107], v[106:107], v[42:43]
	v_pk_add_f32 v[108:109], v[108:109], v[44:45]
	v_pk_add_f32 v[110:111], v[110:111], v[46:47]
	v_pk_add_f32 v[112:113], v[112:113], v[48:49]
	v_pk_add_f32 v[114:115], v[114:115], v[50:51]
	v_pk_add_f32 v[116:117], v[116:117], v[52:53]
	v_pk_add_f32 v[118:119], v[118:119], v[54:55]
	v_pk_add_f32 v[120:121], v[120:121], v[56:57]
	v_pk_add_f32 v[122:123], v[122:123], v[58:59]
	v_pk_add_f32 v[124:125], v[124:125], v[60:61]
	v_pk_add_f32 v[126:127], v[126:127], v[62:63]
	v_pk_add_f32 v[128:129], v[128:129], v[64:65]
	v_pk_add_f32 v[130:131], v[130:131], v[66:67]
	v_pk_add_f32 v[132:133], v[132:133], v[68:69]
	v_pk_add_f32 v[134:135], v[134:135], v[70:71]
	v_pk_add_f32 v[136:137], v[136:137], v[72:73]
	v_pk_add_f32 v[138:139], v[138:139], v[74:75]
	v_pk_add_f32 v[140:141], v[140:141], v[76:77]
	v_pk_add_f32 v[142:143], v[142:143], v[78:79]
	v_pk_add_f32 v[144:145], v[144:145], v[80:81]
	v_pk_add_f32 v[146:147], v[146:147], v[82:83]
	v_pk_add_f32 v[148:149], v[148:149], v[84:85]
	v_pk_add_f32 v[150:151], v[150:151], v[86:87]
	v_pk_add_f32 v[152:153], v[152:153], v[88:89]
	v_pk_add_f32 v[154:155], v[154:155], v[94:95]
	v_pk_add_f32 v[156:157], v[156:157], v[96:97]
	v_pk_add_f32 v[158:159], v[158:159], v[102:103]
	v_pk_add_f32 v[160:161], v[160:161], v[104:105]
	s_branch .Lxk_done
.Lxk_l2:
	s_add_u32 s6, s6, 0x20000
	s_addc_u32 s7, s7, 0
	global_load_dwordx4 v[90:93], v3, s[6:7] sc1
	s_add_u32 s6, s6, 0x2000
	s_addc_u32 s7, s7, 0
	global_load_dwordx4 v[98:101], v3, s[6:7] sc1
	s_add_u32 s6, s6, 0x2000
	s_addc_u32 s7, s7, 0
	global_load_dwordx4 v[106:109], v3, s[6:7] sc1
	s_add_u32 s6, s6, 0x2000
	s_addc_u32 s7, s7, 0
	global_load_dwordx4 v[110:113], v3, s[6:7] sc1
	s_add_u32 s6, s6, 0x2000
	s_addc_u32 s7, s7, 0
	global_load_dwordx4 v[114:117], v3, s[6:7] sc1
	s_add_u32 s6, s6, 0x2000
	s_addc_u32 s7, s7, 0
	global_load_dwordx4 v[118:121], v3, s[6:7] sc1
	s_add_u32 s6, s6, 0x2000
	s_addc_u32 s7, s7, 0
	global_load_dwordx4 v[122:125], v3, s[6:7] sc1
	s_add_u32 s6, s6, 0x2000
	s_addc_u32 s7, s7, 0
	global_load_dwordx4 v[126:129], v3, s[6:7] sc1
	s_add_u32 s6, s6, 0x2000
	s_addc_u32 s7, s7, 0
	global_load_dwordx4 v[130:133], v3, s[6:7] sc1
	s_add_u32 s6, s6, 0x2000
	s_addc_u32 s7, s7, 0
	global_load_dwordx4 v[134:137], v3, s[6:7] sc1
	s_add_u32 s6, s6, 0x2000
	s_addc_u32 s7, s7, 0
	global_load_dwordx4 v[138:141], v3, s[6:7] sc1
	s_add_u32 s6, s6, 0x2000
	s_addc_u32 s7, s7, 0
	global_load_dwordx4 v[142:145], v3, s[6:7] sc1
	s_add_u32 s6, s6, 0x2000
	s_addc_u32 s7, s7, 0
	global_load_dwordx4 v[146:149], v3, s[6:7] sc1
	s_add_u32 s6, s6, 0x2000
	s_addc_u32 s7, s7, 0
	global_load_dwordx4 v[150:153], v3, s[6:7] sc1
	s_add_u32 s6, s6, 0x2000
	s_addc_u32 s7, s7, 0
	global_load_dwordx4 v[154:157], v3, s[6:7] sc1
	s_add_u32 s6, s6, 0x2000
	s_addc_u32 s7, s7, 0
	global_load_dwordx4 v[158:161], v3, s[6:7] sc1
	s_add_u32 s6, s6, 0x2000
	s_addc_u32 s7, s7, 0
	s_waitcnt vmcnt(0)
	v_pk_add_f32 v[34:35], v[34:35], v[90:91]
	v_pk_add_f32 v[36:37], v[36:37], v[92:93]
	v_pk_add_f32 v[38:39], v[38:39], v[98:99]
	v_pk_add_f32 v[40:41], v[40:41], v[100:101]
	v_pk_add_f32 v[42:43], v[42:43], v[106:107]
	v_pk_add_f32 v[44:45], v[44:45], v[108:109]
	v_pk_add_f32 v[46:47], v[46:47], v[110:111]
	v_pk_add_f32 v[48:49], v[48:49], v[112:113]
	v_pk_add_f32 v[50:51], v[50:51], v[114:115]
	v_pk_add_f32 v[52:53], v[52:53], v[116:117]
	v_pk_add_f32 v[54:55], v[54:55], v[118:119]
	v_pk_add_f32 v[56:57], v[56:57], v[120:121]
	v_pk_add_f32 v[58:59], v[58:59], v[122:123]
	v_pk_add_f32 v[60:61], v[60:61], v[124:125]
	v_pk_add_f32 v[62:63], v[62:63], v[126:127]
	v_pk_add_f32 v[64:65], v[64:65], v[128:129]
	v_pk_add_f32 v[66:67], v[66:67], v[130:131]
	v_pk_add_f32 v[68:69], v[68:69], v[132:133]
	v_pk_add_f32 v[70:71], v[70:71], v[134:135]
	v_pk_add_f32 v[72:73], v[72:73], v[136:137]
	v_pk_add_f32 v[74:75], v[74:75], v[138:139]
	v_pk_add_f32 v[76:77], v[76:77], v[140:141]
	v_pk_add_f32 v[78:79], v[78:79], v[142:143]
	v_pk_add_f32 v[80:81], v[80:81], v[144:145]
	v_pk_add_f32 v[82:83], v[82:83], v[146:147]
	v_pk_add_f32 v[84:85], v[84:85], v[148:149]
	v_pk_add_f32 v[86:87], v[86:87], v[150:151]
	v_pk_add_f32 v[88:89], v[88:89], v[152:153]
	v_pk_add_f32 v[94:95], v[94:95], v[154:155]
	v_pk_add_f32 v[96:97], v[96:97], v[156:157]
	v_pk_add_f32 v[102:103], v[102:103], v[158:159]
	v_pk_add_f32 v[104:105], v[104:105], v[160:161]
